# fp8 expert-table conversion served as 512 work-queue units inside P3 (after the 512 heaviest MLA units) instead of in the prologue / P1 tail; same math
# baseline (speedup 1.0000x reference)
.LBB0_298:
	s_or_b64 exec, exec, s[0:1]
	s_mov_b32 s0, s66
	s_mov_b32 s1, s67
	v_writelane_b32 v254, s0, 16
	v_mov_b32_e32 v1, v206
	v_mbcnt_lo_u32_b32 v197, -1, 0
	v_writelane_b32 v254, s1, 17
	v_writelane_b32 v254, s2, 18
	v_writelane_b32 v254, s3, 19
	v_ashrrev_i32_e32 v8, 6, v1
	v_readlane_b32 s0, v254, 12
	v_readlane_b32 s1, v254, 13
	s_nop 0
	v_add_u32_e32 v2, s0, v8
	s_mov_b32 s0, 0
	v_cmp_gt_i32_e32 vcc, s0, v2
	s_and_saveexec_b64 s[0:1], vcc
	s_cbranch_execz .LBB0_307
	v_readlane_b32 s16, v253, 44
	v_readlane_b32 s6, v254, 12
	v_readlane_b32 s17, v253, 45
	v_readlane_b32 s18, v253, 46
	v_readlane_b32 s19, v253, 47
	v_readlane_b32 s28, v253, 56
	v_readlane_b32 s29, v253, 57
	v_ashrrev_i32_e32 v9, 31, v8
	s_mov_b32 s8, s6
	s_ashr_i32 s9, s6, 31
	v_and_b32_e32 v1, 63, v1
	v_mov_b32_e32 v3, 0
	v_readlane_b32 s30, v253, 58
	v_readlane_b32 s31, v253, 59
	s_mov_b64 s[16:17], s[28:29]
	v_readlane_b32 s7, v254, 13
	v_lshl_add_u64 v[8:9], v[8:9], 0, s[8:9]
	v_lshlrev_b32_e32 v10, 6, v1
	v_mov_b32_e32 v11, v3
	v_readlane_b32 s20, v253, 48
	v_readlane_b32 s21, v253, 49
	v_readlane_b32 s22, v253, 50
	v_readlane_b32 s23, v253, 51
	v_readlane_b32 s26, v253, 54
	v_readlane_b32 s27, v253, 55
	s_mov_b64 s[18:19], s[30:31]
	v_writelane_b32 v254, s6, 12
	v_lshlrev_b64 v[12:13], 12, v[8:9]
	s_mov_b64 s[14:15], s[26:27]
	v_lshl_add_u64 v[4:5], s[16:17], 0, v[10:11]
	v_readlane_b32 s16, v253, 0
	v_writelane_b32 v254, s7, 13
	v_or_b32_e32 v12, v12, v10
	v_lshlrev_b32_e32 v2, 4, v1
	v_cmp_eq_u32_e64 s[4:5], 0, v1
	s_lshl_b32 s2, s2, 2
	v_readlane_b32 s17, v253, 1
	v_lshl_add_u64 v[10:11], s[14:15], 0, v[12:13]
	v_lshlrev_b64 v[12:13], 10, v[8:9]
	v_readlane_b32 s8, v254, 16
	v_mbcnt_hi_u32_b32 v1, -1, v197
	v_readlane_b32 s20, v253, 4
	v_lshl_add_u64 v[6:7], s[16:17], 0, v[2:3]
	s_ashr_i32 s3, s2, 31
	v_or_b32_e32 v12, v12, v2
	v_readlane_b32 s9, v254, 17
	v_readlane_b32 s10, v254, 18
	v_readlane_b32 s11, v254, 19
	v_and_b32_e32 v2, 64, v1
	s_lshl_b64 s[6:7], s[2:3], 12
	v_lshl_add_u64 v[12:13], s[8:9], 0, v[12:13]
	s_lshl_b64 s[8:9], s[2:3], 10
	s_mov_b64 s[10:11], 0
	v_add_u32_e32 v18, 64, v2
	v_xor_b32_e32 v19, 1, v1
	v_xor_b32_e32 v20, 2, v1
	v_xor_b32_e32 v21, 4, v1
	v_xor_b32_e32 v22, 8, v1
	v_xor_b32_e32 v23, 16, v1
	v_xor_b32_e32 v24, 32, v1
	s_mov_b32 s20, 0x43e00000
	v_readlane_b32 s24, v253, 52
	v_readlane_b32 s25, v253, 53
	v_readlane_b32 s18, v253, 2
	v_readlane_b32 s19, v253, 3
	v_readlane_b32 s21, v253, 5
	v_readlane_b32 s22, v253, 6
	v_readlane_b32 s23, v253, 7
	s_branch .LBB0_301

.LBB0_453:
	s_andn2_b64 vcc, exec, s[96:97]
	s_branch .LBB0_464
	v_mov_b32_e32 v1, v206
	v_readlane_b32 s0, v254, 12
	v_ashrrev_i32_e32 v4, 6, v1
	v_readlane_b32 s1, v254, 13
	v_add_u32_e32 v2, s0, v4
	s_mov_b32 s0, 0x8000
	v_cmp_gt_i32_e32 vcc, s0, v2
	s_and_saveexec_b64 s[0:1], vcc
	s_cbranch_execz .LBB0_463
	s_load_dword s2, s[94:95], 0x0
	v_and_b32_e32 v1, 63, v1
	v_mov_b32_e32 v7, v3
	v_lshlrev_b32_e32 v6, 6, v1
	v_readlane_b32 s8, v253, 0
	s_waitcnt lgkmcnt(0)
	s_lshl_b32 s6, s2, 2
	v_readlane_b32 s2, v254, 60
	v_readlane_b32 s3, v254, 61
	v_ashrrev_i32_e32 v5, 31, v4
	v_lshlrev_b32_e32 v2, 4, v1
	v_lshl_add_u64 v[24:25], s[2:3], 0, v[6:7]
	v_readlane_b32 s2, v254, 12
	v_readlane_b32 s3, v254, 13
	v_readlane_b32 s9, v253, 1
	v_readlane_b32 s10, v253, 2
	v_readlane_b32 s11, v253, 3
	v_lshl_add_u64 v[28:29], s[2:3], 0, v[4:5]
	v_lshl_add_u64 v[26:27], s[8:9], 0, v[2:3]
	v_lshlrev_b64 v[4:5], 10, v[28:29]
	v_readlane_b32 s8, v254, 16
	v_or_b32_e32 v4, v4, v2
	v_readlane_b32 s9, v254, 17
	v_readlane_b32 s2, v255, 7
	v_readlane_b32 s12, v253, 4
	v_lshl_add_u64 v[30:31], s[8:9], 0, v[4:5]
	v_lshlrev_b64 v[4:5], 12, v[28:29]
	v_readlane_b32 s13, v253, 5
	s_ashr_i32 s7, s6, 31
	v_readlane_b32 s10, v254, 18
	v_readlane_b32 s11, v254, 19
	v_or_b32_e32 v4, v4, v6
	v_readlane_b32 s3, v255, 8
	v_cmp_eq_u32_e64 s[4:5], 0, v1
	s_lshl_b64 s[8:9], s[6:7], 10
	v_lshl_add_u64 v[32:33], s[2:3], 0, v[4:5]
	s_lshl_b64 s[10:11], s[6:7], 12
	s_mov_b64 s[12:13], 0
	v_readlane_b32 s14, v253, 6
	v_readlane_b32 s15, v253, 7
	s_branch .LBB0_457

.Lcvt_unit:
	s_sub_u32 s0, s9, 0x200
	v_readfirstlane_b32 s1, v206
	s_lshr_b32 s1, s1, 6
	s_lshl_b32 s0, s0, 6
	s_lshl_b32 s1, s1, 4
	s_add_i32 s0, s0, s1
	v_mbcnt_lo_u32_b32 v51, -1, 0
	v_mbcnt_hi_u32_b32 v51, -1, v51
	v_lshlrev_b32_e32 v52, 6, v51
	v_lshlrev_b32_e32 v53, 4, v51
	v_mov_b32_e32 v54, 0
	s_cmp_ge_u32 s0, 0x4000
	s_cbranch_scc1 .Lcvt_v
	v_readlane_b32 s2, v253, 54
	v_readlane_b32 s3, v253, 55
	v_readlane_b32 s4, v254, 16
	v_readlane_b32 s5, v254, 17
	v_readlane_b32 s6, v253, 2
	v_readlane_b32 s7, v253, 3
	s_branch .Lcvt_go
.Lcvt_v:
	s_sub_u32 s0, s0, 0x4000
	v_readlane_b32 s2, v253, 56
	v_readlane_b32 s3, v253, 57
	v_readlane_b32 s4, v253, 0
	v_readlane_b32 s5, v253, 1
	v_readlane_b32 s6, v253, 4
	v_readlane_b32 s7, v253, 5
.Lcvt_go:
	s_lshl_b32 s18, s84, 26
	s_add_u32 s2, s2, s18
	s_addc_u32 s3, s3, 0
	s_lshl_b32 s18, s0, 12
	s_add_u32 s2, s2, s18
	s_addc_u32 s3, s3, 0
	s_lshl_b32 s18, s0, 10
	s_add_u32 s4, s4, s18
	s_addc_u32 s5, s5, 0
	s_lshl_b32 s18, s84, 14
	s_add_i32 s18, s18, s0
	s_lshl_b32 s18, s18, 2
	s_add_u32 s6, s6, s18
	s_addc_u32 s7, s7, 0
	s_mov_b32 s19, 0x43e00000
	s_movk_i32 s24, 4
.Lcvt_loop:
	global_load_dwordx4 v[84:87], v52, s[2:3] offset:0
	global_load_dwordx4 v[88:91], v52, s[2:3] offset:16
	global_load_dwordx4 v[92:95], v52, s[2:3] offset:32
	global_load_dwordx4 v[96:99], v52, s[2:3] offset:48
	s_add_u32 s2, s2, 0x1000
	s_addc_u32 s3, s3, 0
	global_load_dwordx4 v[100:103], v52, s[2:3] offset:0
	global_load_dwordx4 v[104:107], v52, s[2:3] offset:16
	global_load_dwordx4 v[108:111], v52, s[2:3] offset:32
	global_load_dwordx4 v[112:115], v52, s[2:3] offset:48
	s_add_u32 s2, s2, 0x1000
	s_addc_u32 s3, s3, 0
	global_load_dwordx4 v[122:125], v52, s[2:3] offset:0
	global_load_dwordx4 v[126:129], v52, s[2:3] offset:16
	global_load_dwordx4 v[130:133], v52, s[2:3] offset:32
	global_load_dwordx4 v[134:137], v52, s[2:3] offset:48
	s_add_u32 s2, s2, 0x1000
	s_addc_u32 s3, s3, 0
	global_load_dwordx4 v[176:179], v52, s[2:3] offset:0
	global_load_dwordx4 v[180:183], v52, s[2:3] offset:16
	global_load_dwordx4 v[184:187], v52, s[2:3] offset:32
	global_load_dwordx4 v[188:191], v52, s[2:3] offset:48
	s_add_u32 s2, s2, 0x1000
	s_addc_u32 s3, s3, 0
	s_waitcnt vmcnt(12)
	v_max3_f32 v55, |v84|, |v85|, |v86|
	v_max3_f32 v55, v55, |v87|, |v88|
	v_max3_f32 v55, v55, |v89|, |v90|
	v_max3_f32 v55, v55, |v91|, |v92|
	v_max3_f32 v55, v55, |v93|, |v94|
	v_max3_f32 v55, v55, |v95|, |v96|
	v_max3_f32 v55, v55, |v97|, |v98|
	v_max_f32_e64 v55, v55, |v99|
	s_nop 1
	v_max_f32_dpp v55, v55, v55 quad_perm:[1,0,3,2] row_mask:0xf bank_mask:0xf
	s_nop 1
	v_max_f32_dpp v55, v55, v55 quad_perm:[2,3,0,1] row_mask:0xf bank_mask:0xf
	s_nop 1
	v_max_f32_dpp v55, v55, v55 row_half_mirror row_mask:0xf bank_mask:0xf
	s_nop 1
	v_max_f32_dpp v55, v55, v55 row_mirror row_mask:0xf bank_mask:0xf
	s_nop 1
	v_readlane_b32 s25, v55, 0
	v_readlane_b32 s26, v55, 16
	v_readlane_b32 s27, v55, 32
	v_readlane_b32 s28, v55, 48
	s_max_u32 s25, s25, s26
	s_max_u32 s27, s27, s28
	s_max_u32 s25, s25, s27
	v_mov_b32_e32 v56, s25
	v_div_scale_f32 v57, s[32:33], v56, v56, s19
	v_rcp_f32_e32 v58, v57
	v_div_scale_f32 v59, vcc, s19, v56, s19
	v_fma_f32 v60, -v57, v58, 1.0
	v_fmac_f32_e32 v58, v60, v58
	v_mul_f32_e32 v60, v59, v58
	v_fma_f32 v61, -v57, v60, v59
	v_fmac_f32_e32 v60, v61, v58
	v_fma_f32 v57, -v57, v60, v59
	v_div_fmas_f32 v57, v57, v58, v60
	v_div_fixup_f32 v57, v57, v56, s19
	v_cmp_lt_f32_e32 vcc, 0, v56
	v_mul_f32_e32 v63, 0x3b124925, v56
	s_nop 0
	v_cndmask_b32_e32 v57, 1.0, v57, vcc
	v_cndmask_b32_e32 v63, 1.0, v63, vcc
	v_mul_f32_e32 v84, v84, v57
	v_mul_f32_e32 v85, v85, v57
	v_mul_f32_e32 v86, v86, v57
	v_mul_f32_e32 v87, v87, v57
	v_mul_f32_e32 v88, v88, v57
	v_mul_f32_e32 v89, v89, v57
	v_mul_f32_e32 v90, v90, v57
	v_mul_f32_e32 v91, v91, v57
	v_mul_f32_e32 v92, v92, v57
	v_mul_f32_e32 v93, v93, v57
	v_mul_f32_e32 v94, v94, v57
	v_mul_f32_e32 v95, v95, v57
	v_mul_f32_e32 v96, v96, v57
	v_mul_f32_e32 v97, v97, v57
	v_mul_f32_e32 v98, v98, v57
	v_mul_f32_e32 v99, v99, v57
	v_cvt_pk_fp8_f32 v64, v84, v85
	v_cvt_pk_fp8_f32 v64, v86, v87 op_sel:[0,0,1]
	v_cvt_pk_fp8_f32 v65, v88, v89
	v_cvt_pk_fp8_f32 v65, v90, v91 op_sel:[0,0,1]
	v_cvt_pk_fp8_f32 v66, v92, v93
	v_cvt_pk_fp8_f32 v66, v94, v95 op_sel:[0,0,1]
	v_cvt_pk_fp8_f32 v67, v96, v97
	v_cvt_pk_fp8_f32 v67, v98, v99 op_sel:[0,0,1]
	global_store_dwordx4 v53, v[64:67], s[4:5]
	s_mov_b64 s[30:31], exec
	s_mov_b64 exec, 1
	global_store_dword v54, v63, s[6:7]
	s_mov_b64 exec, s[30:31]
	s_add_u32 s4, s4, 0x400
	s_addc_u32 s5, s5, 0
	s_add_u32 s6, s6, 4
	s_addc_u32 s7, s7, 0
	s_waitcnt vmcnt(10)
	v_max3_f32 v55, |v100|, |v101|, |v102|
	v_max3_f32 v55, v55, |v103|, |v104|
	v_max3_f32 v55, v55, |v105|, |v106|
	v_max3_f32 v55, v55, |v107|, |v108|
	v_max3_f32 v55, v55, |v109|, |v110|
	v_max3_f32 v55, v55, |v111|, |v112|
	v_max3_f32 v55, v55, |v113|, |v114|
	v_max_f32_e64 v55, v55, |v115|
	s_nop 1
	v_max_f32_dpp v55, v55, v55 quad_perm:[1,0,3,2] row_mask:0xf bank_mask:0xf
	s_nop 1
	v_max_f32_dpp v55, v55, v55 quad_perm:[2,3,0,1] row_mask:0xf bank_mask:0xf
	s_nop 1
	v_max_f32_dpp v55, v55, v55 row_half_mirror row_mask:0xf bank_mask:0xf
	s_nop 1
	v_max_f32_dpp v55, v55, v55 row_mirror row_mask:0xf bank_mask:0xf
	s_nop 1
	v_readlane_b32 s25, v55, 0
	v_readlane_b32 s26, v55, 16
	v_readlane_b32 s27, v55, 32
	v_readlane_b32 s28, v55, 48
	s_max_u32 s25, s25, s26
	s_max_u32 s27, s27, s28
	s_max_u32 s25, s25, s27
	v_mov_b32_e32 v56, s25
	v_div_scale_f32 v57, s[32:33], v56, v56, s19
	v_rcp_f32_e32 v58, v57
	v_div_scale_f32 v59, vcc, s19, v56, s19
	v_fma_f32 v60, -v57, v58, 1.0
	v_fmac_f32_e32 v58, v60, v58
	v_mul_f32_e32 v60, v59, v58
	v_fma_f32 v61, -v57, v60, v59
	v_fmac_f32_e32 v60, v61, v58
	v_fma_f32 v57, -v57, v60, v59
	v_div_fmas_f32 v57, v57, v58, v60
	v_div_fixup_f32 v57, v57, v56, s19
	v_cmp_lt_f32_e32 vcc, 0, v56
	v_mul_f32_e32 v63, 0x3b124925, v56
	s_nop 0
	v_cndmask_b32_e32 v57, 1.0, v57, vcc
	v_cndmask_b32_e32 v63, 1.0, v63, vcc
	v_mul_f32_e32 v100, v100, v57
	v_mul_f32_e32 v101, v101, v57
	v_mul_f32_e32 v102, v102, v57
	v_mul_f32_e32 v103, v103, v57
	v_mul_f32_e32 v104, v104, v57
	v_mul_f32_e32 v105, v105, v57
	v_mul_f32_e32 v106, v106, v57
	v_mul_f32_e32 v107, v107, v57
	v_mul_f32_e32 v108, v108, v57
	v_mul_f32_e32 v109, v109, v57
	v_mul_f32_e32 v110, v110, v57
	v_mul_f32_e32 v111, v111, v57
	v_mul_f32_e32 v112, v112, v57
	v_mul_f32_e32 v113, v113, v57
	v_mul_f32_e32 v114, v114, v57
	v_mul_f32_e32 v115, v115, v57
	v_cvt_pk_fp8_f32 v68, v100, v101
	v_cvt_pk_fp8_f32 v68, v102, v103 op_sel:[0,0,1]
	v_cvt_pk_fp8_f32 v69, v104, v105
	v_cvt_pk_fp8_f32 v69, v106, v107 op_sel:[0,0,1]
	v_cvt_pk_fp8_f32 v70, v108, v109
	v_cvt_pk_fp8_f32 v70, v110, v111 op_sel:[0,0,1]
	v_cvt_pk_fp8_f32 v71, v112, v113
	v_cvt_pk_fp8_f32 v71, v114, v115 op_sel:[0,0,1]
	global_store_dwordx4 v53, v[68:71], s[4:5]
	s_mov_b64 s[30:31], exec
	s_mov_b64 exec, 1
	global_store_dword v54, v63, s[6:7]
	s_mov_b64 exec, s[30:31]
	s_add_u32 s4, s4, 0x400
	s_addc_u32 s5, s5, 0
	s_add_u32 s6, s6, 4
	s_addc_u32 s7, s7, 0
	s_waitcnt vmcnt(8)
	v_max3_f32 v55, |v122|, |v123|, |v124|
	v_max3_f32 v55, v55, |v125|, |v126|
	v_max3_f32 v55, v55, |v127|, |v128|
	v_max3_f32 v55, v55, |v129|, |v130|
	v_max3_f32 v55, v55, |v131|, |v132|
	v_max3_f32 v55, v55, |v133|, |v134|
	v_max3_f32 v55, v55, |v135|, |v136|
	v_max_f32_e64 v55, v55, |v137|
	s_nop 1
	v_max_f32_dpp v55, v55, v55 quad_perm:[1,0,3,2] row_mask:0xf bank_mask:0xf
	s_nop 1
	v_max_f32_dpp v55, v55, v55 quad_perm:[2,3,0,1] row_mask:0xf bank_mask:0xf
	s_nop 1
	v_max_f32_dpp v55, v55, v55 row_half_mirror row_mask:0xf bank_mask:0xf
	s_nop 1
	v_max_f32_dpp v55, v55, v55 row_mirror row_mask:0xf bank_mask:0xf
	s_nop 1
	v_readlane_b32 s25, v55, 0
	v_readlane_b32 s26, v55, 16
	v_readlane_b32 s27, v55, 32
	v_readlane_b32 s28, v55, 48
	s_max_u32 s25, s25, s26
	s_max_u32 s27, s27, s28
	s_max_u32 s25, s25, s27
	v_mov_b32_e32 v56, s25
	v_div_scale_f32 v57, s[32:33], v56, v56, s19
	v_rcp_f32_e32 v58, v57
	v_div_scale_f32 v59, vcc, s19, v56, s19
	v_fma_f32 v60, -v57, v58, 1.0
	v_fmac_f32_e32 v58, v60, v58
	v_mul_f32_e32 v60, v59, v58
	v_fma_f32 v61, -v57, v60, v59
	v_fmac_f32_e32 v60, v61, v58
	v_fma_f32 v57, -v57, v60, v59
	v_div_fmas_f32 v57, v57, v58, v60
	v_div_fixup_f32 v57, v57, v56, s19
	v_cmp_lt_f32_e32 vcc, 0, v56
	v_mul_f32_e32 v63, 0x3b124925, v56
	s_nop 0
	v_cndmask_b32_e32 v57, 1.0, v57, vcc
	v_cndmask_b32_e32 v63, 1.0, v63, vcc
	v_mul_f32_e32 v122, v122, v57
	v_mul_f32_e32 v123, v123, v57
	v_mul_f32_e32 v124, v124, v57
	v_mul_f32_e32 v125, v125, v57
	v_mul_f32_e32 v126, v126, v57
	v_mul_f32_e32 v127, v127, v57
	v_mul_f32_e32 v128, v128, v57
	v_mul_f32_e32 v129, v129, v57
	v_mul_f32_e32 v130, v130, v57
	v_mul_f32_e32 v131, v131, v57
	v_mul_f32_e32 v132, v132, v57
	v_mul_f32_e32 v133, v133, v57
	v_mul_f32_e32 v134, v134, v57
	v_mul_f32_e32 v135, v135, v57
	v_mul_f32_e32 v136, v136, v57
	v_mul_f32_e32 v137, v137, v57
	v_cvt_pk_fp8_f32 v72, v122, v123
	v_cvt_pk_fp8_f32 v72, v124, v125 op_sel:[0,0,1]
	v_cvt_pk_fp8_f32 v73, v126, v127
	v_cvt_pk_fp8_f32 v73, v128, v129 op_sel:[0,0,1]
	v_cvt_pk_fp8_f32 v74, v130, v131
	v_cvt_pk_fp8_f32 v74, v132, v133 op_sel:[0,0,1]
	v_cvt_pk_fp8_f32 v75, v134, v135
	v_cvt_pk_fp8_f32 v75, v136, v137 op_sel:[0,0,1]
	global_store_dwordx4 v53, v[72:75], s[4:5]
	s_mov_b64 s[30:31], exec
	s_mov_b64 exec, 1
	global_store_dword v54, v63, s[6:7]
	s_mov_b64 exec, s[30:31]
	s_add_u32 s4, s4, 0x400
	s_addc_u32 s5, s5, 0
	s_add_u32 s6, s6, 4
	s_addc_u32 s7, s7, 0
	s_waitcnt vmcnt(6)
	v_max3_f32 v55, |v176|, |v177|, |v178|
	v_max3_f32 v55, v55, |v179|, |v180|
	v_max3_f32 v55, v55, |v181|, |v182|
	v_max3_f32 v55, v55, |v183|, |v184|
	v_max3_f32 v55, v55, |v185|, |v186|
	v_max3_f32 v55, v55, |v187|, |v188|
	v_max3_f32 v55, v55, |v189|, |v190|
	v_max_f32_e64 v55, v55, |v191|
	s_nop 1
	v_max_f32_dpp v55, v55, v55 quad_perm:[1,0,3,2] row_mask:0xf bank_mask:0xf
	s_nop 1
	v_max_f32_dpp v55, v55, v55 quad_perm:[2,3,0,1] row_mask:0xf bank_mask:0xf
	s_nop 1
	v_max_f32_dpp v55, v55, v55 row_half_mirror row_mask:0xf bank_mask:0xf
	s_nop 1
	v_max_f32_dpp v55, v55, v55 row_mirror row_mask:0xf bank_mask:0xf
	s_nop 1
	v_readlane_b32 s25, v55, 0
	v_readlane_b32 s26, v55, 16
	v_readlane_b32 s27, v55, 32
	v_readlane_b32 s28, v55, 48
	s_max_u32 s25, s25, s26
	s_max_u32 s27, s27, s28
	s_max_u32 s25, s25, s27
	v_mov_b32_e32 v56, s25
	v_div_scale_f32 v57, s[32:33], v56, v56, s19
	v_rcp_f32_e32 v58, v57
	v_div_scale_f32 v59, vcc, s19, v56, s19
	v_fma_f32 v60, -v57, v58, 1.0
	v_fmac_f32_e32 v58, v60, v58
	v_mul_f32_e32 v60, v59, v58
	v_fma_f32 v61, -v57, v60, v59
	v_fmac_f32_e32 v60, v61, v58
	v_fma_f32 v57, -v57, v60, v59
	v_div_fmas_f32 v57, v57, v58, v60
	v_div_fixup_f32 v57, v57, v56, s19
	v_cmp_lt_f32_e32 vcc, 0, v56
	v_mul_f32_e32 v63, 0x3b124925, v56
	s_nop 0
	v_cndmask_b32_e32 v57, 1.0, v57, vcc
	v_cndmask_b32_e32 v63, 1.0, v63, vcc
	v_mul_f32_e32 v176, v176, v57
	v_mul_f32_e32 v177, v177, v57
	v_mul_f32_e32 v178, v178, v57
	v_mul_f32_e32 v179, v179, v57
	v_mul_f32_e32 v180, v180, v57
	v_mul_f32_e32 v181, v181, v57
	v_mul_f32_e32 v182, v182, v57
	v_mul_f32_e32 v183, v183, v57
	v_mul_f32_e32 v184, v184, v57
	v_mul_f32_e32 v185, v185, v57
	v_mul_f32_e32 v186, v186, v57
	v_mul_f32_e32 v187, v187, v57
	v_mul_f32_e32 v188, v188, v57
	v_mul_f32_e32 v189, v189, v57
	v_mul_f32_e32 v190, v190, v57
	v_mul_f32_e32 v191, v191, v57
	v_cvt_pk_fp8_f32 v76, v176, v177
	v_cvt_pk_fp8_f32 v76, v178, v179 op_sel:[0,0,1]
	v_cvt_pk_fp8_f32 v77, v180, v181
	v_cvt_pk_fp8_f32 v77, v182, v183 op_sel:[0,0,1]
	v_cvt_pk_fp8_f32 v78, v184, v185
	v_cvt_pk_fp8_f32 v78, v186, v187 op_sel:[0,0,1]
	v_cvt_pk_fp8_f32 v79, v188, v189
	v_cvt_pk_fp8_f32 v79, v190, v191 op_sel:[0,0,1]
	global_store_dwordx4 v53, v[76:79], s[4:5]
	s_mov_b64 s[30:31], exec
	s_mov_b64 exec, 1
	global_store_dword v54, v63, s[6:7]
	s_mov_b64 exec, s[30:31]
	s_add_u32 s4, s4, 0x400
	s_addc_u32 s5, s5, 0
	s_add_u32 s6, s6, 4
	s_addc_u32 s7, s7, 0
	s_add_i32 s24, s24, -1
	s_cmp_lg_u32 s24, 0
	s_cbranch_scc1 .Lcvt_loop
	s_branch .LBB0_610

.LBB0_616:
	s_or_b64 exec, exec, s[0:1]
	v_readlane_b32 s0, v255, 21
	s_waitcnt lgkmcnt(0)
	s_barrier
	v_mov_b32_e32 v1, s0
	ds_read_b32 v1, v1
	s_movk_i32 s0, 0xdff
	s_waitcnt lgkmcnt(0)
	v_cmp_lt_i32_e32 vcc, s0, v1
	v_readfirstlane_b32 s9, v1
	s_cmpk_lt_u32 s9, 0x200
	s_cbranch_scc1 .Lq_keep
	s_cmpk_ge_u32 s9, 0xe00
	s_cbranch_scc1 .Lq_keep
	s_cmpk_lt_u32 s9, 0x400
	s_cbranch_scc1 .Lcvt_unit
	s_addk_i32 s9, 0xfe00
.Lq_keep:
	s_mov_b64 s[0:1], -1
	s_cbranch_vccnz .LBB0_611
	s_cmpk_gt_i32 s9, 0x3ff
	s_cbranch_scc0 .LBB0_624
	s_cmpk_gt_u32 s9, 0x7ff
	s_mov_b64 s[18:19], s[42:43]
	s_cbranch_scc0 .LBB0_630
	v_mov_b32_e32 v12, v206
	s_movk_i32 s0, 0x7c0
	s_lshl_b32 s20, s9, 5
	v_cmp_gt_i32_e32 vcc, s0, v12
	s_barrier
	s_and_saveexec_b64 s[0:1], vcc
	s_cbranch_execz .LBB0_625
	s_and_b32 s2, s20, 0x1fe0
	s_sub_i32 s2, 29, s2
	s_add_i32 s3, s20, 0xfffeffe2
	v_lshlrev_b32_e32 v1, 3, v12
	s_mov_b64 s[14:15], 0
	v_mov_b32_e32 v8, v12
	s_branch .LBB0_622
